# hcat phase: the per-group shift/scale table is built with all 68 loads of a thread in flight and one wait (was four dependent round trips), same summation order
# speedup vs baseline: 1.0083x; 1.0041x over previous
.Lada_wait_skip:
	s_barrier
	s_load_dwordx2 s[28:29], s[12:13], 0x28
	s_ashr_i32 s39, s37, 7
	s_mul_i32 s40, s39, 0x6000
	v_lshlrev_b32_e32 v144, 2, v186
	v_add_u32_e32 v145, 0x1000, v144
	s_add_u32 s60, s14, s40
	s_addc_u32 s61, s15, 0
	s_add_u32 s76, s14, 0xc000
	s_addc_u32 s77, s15, 0
	s_add_u32 s62, s60, 0x12000
	s_addc_u32 s63, s61, 0
	s_add_u32 s78, s76, 0x12000
	s_addc_u32 s79, s77, 0
	s_add_u32 s64, s62, 0x12000
	s_addc_u32 s65, s63, 0
	s_add_u32 s80, s78, 0x12000
	s_addc_u32 s81, s79, 0
	s_add_u32 s66, s64, 0x12000
	s_addc_u32 s67, s65, 0
	s_add_u32 s82, s80, 0x12000
	s_addc_u32 s83, s81, 0
	s_add_u32 s68, s66, 0x12000
	s_addc_u32 s69, s67, 0
	s_add_u32 s84, s82, 0x12000
	s_addc_u32 s85, s83, 0
	s_add_u32 s70, s68, 0x12000
	s_addc_u32 s71, s69, 0
	s_add_u32 s86, s84, 0x12000
	s_addc_u32 s87, s85, 0
	s_add_u32 s72, s70, 0x12000
	s_addc_u32 s73, s71, 0
	s_add_u32 s88, s86, 0x12000
	s_addc_u32 s89, s87, 0
	s_add_u32 s74, s72, 0x12000
	s_addc_u32 s75, s73, 0
	s_add_u32 s90, s88, 0x12000
	s_addc_u32 s91, s89, 0
	s_waitcnt lgkmcnt(0)
	global_load_dword v146, v144, s[28:29]
	global_load_dword v147, v144, s[28:29] offset:2048
	global_load_dword v150, v145, s[28:29]
	global_load_dword v161, v145, s[28:29] offset:2048
	global_load_dword v163, v144, s[60:61]
	global_load_dword v165, v144, s[60:61] offset:2048
	global_load_dword v174, v145, s[60:61]
	global_load_dword v175, v145, s[60:61] offset:2048
	global_load_dword v176, v144, s[62:63]
	global_load_dword v177, v144, s[62:63] offset:2048
	global_load_dword v178, v145, s[62:63]
	global_load_dword v179, v145, s[62:63] offset:2048
	global_load_dword v180, v144, s[64:65]
	global_load_dword v182, v144, s[64:65] offset:2048
	global_load_dword v184, v145, s[64:65]
	global_load_dword v201, v145, s[64:65] offset:2048
	global_load_dword v202, v144, s[66:67]
	global_load_dword v203, v144, s[66:67] offset:2048
	global_load_dword v204, v145, s[66:67]
	global_load_dword v205, v145, s[66:67] offset:2048
	global_load_dword v206, v144, s[68:69]
	global_load_dword v207, v144, s[68:69] offset:2048
	global_load_dword v208, v145, s[68:69]
	global_load_dword v209, v145, s[68:69] offset:2048
	global_load_dword v210, v144, s[70:71]
	global_load_dword v211, v144, s[70:71] offset:2048
	global_load_dword v212, v145, s[70:71]
	global_load_dword v213, v145, s[70:71] offset:2048
	global_load_dword v214, v144, s[72:73]
	global_load_dword v215, v144, s[72:73] offset:2048
	global_load_dword v216, v145, s[72:73]
	global_load_dword v217, v145, s[72:73] offset:2048
	global_load_dword v218, v144, s[74:75]
	global_load_dword v219, v144, s[74:75] offset:2048
	global_load_dword v220, v145, s[74:75]
	global_load_dword v221, v145, s[74:75] offset:2048
	global_load_dword v222, v144, s[76:77]
	global_load_dword v223, v144, s[76:77] offset:2048
	global_load_dword v224, v145, s[76:77]
	global_load_dword v225, v145, s[76:77] offset:2048
	global_load_dword v226, v144, s[78:79]
	global_load_dword v227, v144, s[78:79] offset:2048
	global_load_dword v228, v145, s[78:79]
	global_load_dword v229, v145, s[78:79] offset:2048
	global_load_dword v230, v144, s[80:81]
	global_load_dword v231, v144, s[80:81] offset:2048
	global_load_dword v232, v145, s[80:81]
	global_load_dword v233, v145, s[80:81] offset:2048
	global_load_dword v234, v144, s[82:83]
	global_load_dword v236, v144, s[82:83] offset:2048
	global_load_dword v237, v145, s[82:83]
	global_load_dword v238, v145, s[82:83] offset:2048
	global_load_dword v239, v144, s[84:85]
	global_load_dword v240, v144, s[84:85] offset:2048
	global_load_dword v241, v145, s[84:85]
	global_load_dword v242, v145, s[84:85] offset:2048
	global_load_dword v243, v144, s[86:87]
	global_load_dword v244, v144, s[86:87] offset:2048
	global_load_dword v245, v145, s[86:87]
	global_load_dword v246, v145, s[86:87] offset:2048
	global_load_dword v247, v144, s[88:89]
	global_load_dword v248, v144, s[88:89] offset:2048
	global_load_dword v249, v145, s[88:89]
	global_load_dword v250, v145, s[88:89] offset:2048
	global_load_dword v251, v144, s[90:91]
	global_load_dword v252, v144, s[90:91] offset:2048
	global_load_dword v253, v145, s[90:91]
	global_load_dword v254, v145, s[90:91] offset:2048
	s_waitcnt vmcnt(0)
	v_add_f32_e32 v163, v146, v163
	v_add_f32_e32 v222, v146, v222
	v_add_f32_e32 v165, v147, v165
	v_add_f32_e32 v223, v147, v223
	v_add_f32_e32 v174, v150, v174
	v_add_f32_e32 v224, v150, v224
	v_add_f32_e32 v175, v161, v175
	v_add_f32_e32 v225, v161, v225
	v_add_f32_e32 v163, v163, v176
	v_add_f32_e32 v222, v222, v226
	v_add_f32_e32 v165, v165, v177
	v_add_f32_e32 v223, v223, v227
	v_add_f32_e32 v174, v174, v178
	v_add_f32_e32 v224, v224, v228
	v_add_f32_e32 v175, v175, v179
	v_add_f32_e32 v225, v225, v229
	v_add_f32_e32 v163, v163, v180
	v_add_f32_e32 v222, v222, v230
	v_add_f32_e32 v165, v165, v182
	v_add_f32_e32 v223, v223, v231
	v_add_f32_e32 v174, v174, v184
	v_add_f32_e32 v224, v224, v232
	v_add_f32_e32 v175, v175, v201
	v_add_f32_e32 v225, v225, v233
	v_add_f32_e32 v163, v163, v202
	v_add_f32_e32 v222, v222, v234
	v_add_f32_e32 v165, v165, v203
	v_add_f32_e32 v223, v223, v236
	v_add_f32_e32 v174, v174, v204
	v_add_f32_e32 v224, v224, v237
	v_add_f32_e32 v175, v175, v205
	v_add_f32_e32 v225, v225, v238
	v_add_f32_e32 v163, v163, v206
	v_add_f32_e32 v222, v222, v239
	v_add_f32_e32 v165, v165, v207
	v_add_f32_e32 v223, v223, v240
	v_add_f32_e32 v174, v174, v208
	v_add_f32_e32 v224, v224, v241
	v_add_f32_e32 v175, v175, v209
	v_add_f32_e32 v225, v225, v242
	v_add_f32_e32 v163, v163, v210
	v_add_f32_e32 v222, v222, v243
	v_add_f32_e32 v165, v165, v211
	v_add_f32_e32 v223, v223, v244
	v_add_f32_e32 v174, v174, v212
	v_add_f32_e32 v224, v224, v245
	v_add_f32_e32 v175, v175, v213
	v_add_f32_e32 v225, v225, v246
	v_add_f32_e32 v163, v163, v214
	v_add_f32_e32 v222, v222, v247
	v_add_f32_e32 v165, v165, v215
	v_add_f32_e32 v223, v223, v248
	v_add_f32_e32 v174, v174, v216
	v_add_f32_e32 v224, v224, v249
	v_add_f32_e32 v175, v175, v217
	v_add_f32_e32 v225, v225, v250
	v_add_f32_e32 v163, v163, v218
	v_add_f32_e32 v222, v222, v251
	v_add_f32_e32 v165, v165, v219
	v_add_f32_e32 v223, v223, v252
	v_add_f32_e32 v174, v174, v220
	v_add_f32_e32 v224, v224, v253
	v_add_f32_e32 v175, v175, v221
	v_add_f32_e32 v225, v225, v254
	ds_write_b32 v144, v163
	ds_write_b32 v144, v222 offset:8192
	ds_write_b32 v144, v165 offset:2048
	ds_write_b32 v144, v223 offset:10240
	ds_write_b32 v144, v174 offset:4096
	ds_write_b32 v144, v224 offset:12288
	ds_write_b32 v144, v175 offset:6144
	ds_write_b32 v144, v225 offset:14336
	s_waitcnt lgkmcnt(0)
	s_waitcnt vmcnt(35)
	v_mov_b32_e32 v146, v129
	s_waitcnt vmcnt(34)
	v_mov_b32_e32 v147, v125
	v_mov_b32_e32 v144, v128
	v_mov_b32_e32 v145, v124
	v_pk_mul_f32 v[146:147], v[146:147], v[146:147]
	s_waitcnt vmcnt(33)
	v_mov_b32_e32 v174, v97
	v_pk_fma_f32 v[144:145], v[144:145], v[144:145], v[146:147]
	v_mov_b32_e32 v146, v130
	v_mov_b32_e32 v147, v126
	v_pk_fma_f32 v[144:145], v[146:147], v[146:147], v[144:145]
	v_mov_b32_e32 v146, v131
	v_mov_b32_e32 v147, v127
	s_waitcnt vmcnt(32)
	v_mov_b32_e32 v175, v85
	v_pk_fma_f32 v[144:145], v[146:147], v[146:147], v[144:145]
	v_mov_b32_e32 v146, v96
	v_mov_b32_e32 v147, v84
	v_pk_mul_f32 v[174:175], v[174:175], v[174:175]
	s_waitcnt vmcnt(31)
	v_mov_b32_e32 v176, v133
	v_pk_fma_f32 v[146:147], v[146:147], v[146:147], v[174:175]
	v_mov_b32_e32 v174, v98
	v_mov_b32_e32 v175, v86
	v_pk_fma_f32 v[146:147], v[174:175], v[174:175], v[146:147]
	v_mov_b32_e32 v174, v99
	v_mov_b32_e32 v175, v87
	s_waitcnt vmcnt(30)
	v_mov_b32_e32 v177, v113
	v_pk_fma_f32 v[146:147], v[174:175], v[174:175], v[146:147]
	v_mov_b32_e32 v174, v132
	v_mov_b32_e32 v175, v112
	v_pk_mul_f32 v[176:177], v[176:177], v[176:177]
	s_waitcnt vmcnt(29)
	v_mov_b32_e32 v178, v101
	v_pk_fma_f32 v[174:175], v[174:175], v[174:175], v[176:177]
	v_mov_b32_e32 v176, v134
	v_mov_b32_e32 v177, v114
	v_pk_fma_f32 v[174:175], v[176:177], v[176:177], v[174:175]
	v_mov_b32_e32 v176, v135
	v_mov_b32_e32 v177, v115
	s_waitcnt vmcnt(28)
	v_mov_b32_e32 v179, v89
	v_pk_fma_f32 v[174:175], v[176:177], v[176:177], v[174:175]
	v_mov_b32_e32 v176, v100
	v_mov_b32_e32 v177, v88
	v_pk_mul_f32 v[178:179], v[178:179], v[178:179]
	s_waitcnt vmcnt(23)
	v_mov_b32_e32 v202, v141
	v_pk_fma_f32 v[176:177], v[176:177], v[176:177], v[178:179]
	v_mov_b32_e32 v178, v102
	v_mov_b32_e32 v179, v90
	v_pk_fma_f32 v[176:177], v[178:179], v[178:179], v[176:177]
	v_mov_b32_e32 v178, v103
	v_mov_b32_e32 v179, v91
	v_pk_fma_f32 v[176:177], v[178:179], v[178:179], v[176:177]
	v_mov_b32_e32 v178, v174
	v_mov_b32_e32 v179, v144
	v_mov_b32_e32 v144, v175
	v_pk_add_f32 v[144:145], v[178:179], v[144:145]
	v_mov_b32_e32 v174, v176
	v_mov_b32_e32 v175, v146
	v_mov_b32_e32 v146, v177
	v_mov_b32_e32 v176, v137
	v_mov_b32_e32 v177, v117
	v_pk_add_f32 v[144:145], v[144:145], v[174:175]
	v_mov_b32_e32 v174, v136
	v_mov_b32_e32 v175, v116
	v_pk_mul_f32 v[176:177], v[176:177], v[176:177]
	v_mov_b32_e32 v178, v105
	v_pk_fma_f32 v[174:175], v[174:175], v[174:175], v[176:177]
	v_mov_b32_e32 v176, v138
	v_mov_b32_e32 v177, v118
	v_pk_fma_f32 v[174:175], v[176:177], v[176:177], v[174:175]
	v_mov_b32_e32 v176, v139
	v_mov_b32_e32 v177, v119
	v_mov_b32_e32 v179, v93
	v_pk_fma_f32 v[174:175], v[176:177], v[176:177], v[174:175]
	v_mov_b32_e32 v176, v104
	v_mov_b32_e32 v177, v92
	v_pk_mul_f32 v[178:179], v[178:179], v[178:179]
	s_waitcnt vmcnt(22)
	v_mov_b32_e32 v203, v121
	v_pk_fma_f32 v[176:177], v[176:177], v[176:177], v[178:179]
	v_mov_b32_e32 v178, v106
	v_mov_b32_e32 v179, v94
	v_pk_fma_f32 v[176:177], v[178:179], v[178:179], v[176:177]
	v_mov_b32_e32 v178, v107
	v_mov_b32_e32 v179, v95
	v_pk_fma_f32 v[176:177], v[178:179], v[178:179], v[176:177]
	v_mov_b32_e32 v178, v140
	v_mov_b32_e32 v179, v120
	v_pk_mul_f32 v[202:203], v[202:203], v[202:203]
	s_waitcnt lgkmcnt(0)
	v_pk_fma_f32 v[178:179], v[178:179], v[178:179], v[202:203]
	v_mov_b32_e32 v202, v142
	v_mov_b32_e32 v203, v122
	v_pk_fma_f32 v[178:179], v[202:203], v[202:203], v[178:179]
	v_mov_b32_e32 v202, v143
	v_mov_b32_e32 v203, v123
	s_barrier
	v_pk_fma_f32 v[178:179], v[202:203], v[202:203], v[178:179]
	global_load_dwordx4 v[202:205], v[156:157], off
	v_pk_add_f32 v[144:145], v[144:145], v[146:147]
	ds_bpermute_b32 v147, v189, v145
	ds_bpermute_b32 v146, v189, v144
	s_waitcnt vmcnt(22)
	v_mov_b32_e32 v208, v109
	s_waitcnt vmcnt(21)
	v_mov_b32_e32 v209, v81
	v_mov_b32_e32 v206, v108
	v_mov_b32_e32 v207, v80
	s_waitcnt lgkmcnt(0)
	v_pk_add_f32 v[144:145], v[144:145], v[146:147]
	ds_bpermute_b32 v147, v190, v145
	ds_bpermute_b32 v146, v190, v144
	v_pk_mul_f32 v[208:209], v[208:209], v[208:209]
	v_lshlrev_b64 v[168:169], 11, v[168:169]
	v_pk_fma_f32 v[206:207], v[206:207], v[206:207], v[208:209]
	v_mov_b32_e32 v208, v110
	s_waitcnt lgkmcnt(0)
	v_pk_add_f32 v[144:145], v[144:145], v[146:147]
	ds_bpermute_b32 v147, v191, v145
	ds_bpermute_b32 v146, v191, v144
	v_mov_b32_e32 v209, v82
	v_pk_fma_f32 v[206:207], v[208:209], v[208:209], v[206:207]
	v_mov_b32_e32 v208, v111
	v_mov_b32_e32 v209, v83
	v_pk_fma_f32 v[206:207], v[208:209], v[208:209], v[206:207]
	v_mov_b32_e32 v208, v178
	v_mov_b32_e32 v209, v174
	v_mov_b32_e32 v174, v179
	v_pk_add_f32 v[174:175], v[208:209], v[174:175]
	v_mov_b32_e32 v178, v206
	v_mov_b32_e32 v179, v176
	v_pk_add_f32 v[174:175], v[174:175], v[178:179]
	v_mov_b32_e32 v176, v207
	s_waitcnt lgkmcnt(0)
	v_pk_add_f32 v[144:145], v[144:145], v[146:147]
	v_pk_add_f32 v[174:175], v[174:175], v[176:177]
	ds_bpermute_b32 v147, v192, v145
	ds_bpermute_b32 v146, v192, v144
	ds_bpermute_b32 v177, v189, v175
	ds_bpermute_b32 v176, v189, v174
	ds_read_b128 v[206:209], v196 offset:4096
	v_lshlrev_b64 v[170:171], 11, v[170:171]
	s_waitcnt lgkmcnt(3)
	v_pk_add_f32 v[144:145], v[144:145], v[146:147]
	ds_bpermute_b32 v147, v193, v145
	s_waitcnt lgkmcnt(2)
	v_pk_add_f32 v[174:175], v[174:175], v[176:177]
	ds_bpermute_b32 v146, v193, v144
	ds_bpermute_b32 v177, v190, v175
	ds_bpermute_b32 v176, v190, v174
	v_mov_b32_e32 v165, v151
	s_waitcnt lgkmcnt(2)
	v_pk_add_f32 v[144:145], v[144:145], v[146:147]
	ds_bpermute_b32 v147, v194, v145
	s_waitcnt lgkmcnt(1)
	v_pk_add_f32 v[176:177], v[174:175], v[176:177]
	ds_bpermute_b32 v146, v194, v144
	ds_bpermute_b32 v179, v191, v177
	ds_bpermute_b32 v178, v191, v176
	v_mov_b64_e32 v[174:175], s[22:23]
	s_waitcnt lgkmcnt(2)
	v_pk_add_f32 v[144:145], v[144:145], v[146:147]
	s_nop 0
	v_pk_fma_f32 v[144:145], v[144:145], s[20:21], v[174:175] op_sel_hi:[1,0,0]
	s_waitcnt lgkmcnt(0)
	v_pk_add_f32 v[146:147], v[176:177], v[178:179]
	ds_bpermute_b32 v177, v192, v147
	ds_bpermute_b32 v176, v192, v146
	v_mul_f32_e32 v150, 0x4b800000, v145
	v_cmp_gt_f32_e64 s[0:1], s36, v145
	v_cmp_gt_f32_e64 s[2:3], s36, v144
	v_pk_add_f32 v[178:179], v[206:207], 1.0 op_sel_hi:[1,0]
	s_waitcnt lgkmcnt(0)
	v_pk_add_f32 v[146:147], v[146:147], v[176:177]
	ds_bpermute_b32 v177, v193, v147
	ds_bpermute_b32 v176, v193, v146
	v_cndmask_b32_e64 v145, v145, v150, s[0:1]
	v_rsq_f32_e32 v150, v145
	v_mul_f32_e32 v145, 0x4b800000, v144
	v_cndmask_b32_e64 v144, v144, v145, s[2:3]
	v_rsq_f32_e32 v161, v144
	s_waitcnt lgkmcnt(0)
	v_pk_add_f32 v[144:145], v[146:147], v[176:177]
	ds_bpermute_b32 v147, v194, v145
	ds_bpermute_b32 v146, v194, v144
	v_mul_f32_e32 v163, 0x45800000, v150
	v_cndmask_b32_e64 v180, v150, v163, s[0:1]
	v_mul_f32_e32 v150, 0x45800000, v161
	v_cndmask_b32_e64 v182, v161, v150, s[2:3]
	s_waitcnt lgkmcnt(0)
	v_pk_add_f32 v[144:145], v[144:145], v[146:147]
	v_pk_add_f32 v[176:177], v[208:209], 1.0 op_sel_hi:[1,0]
	v_pk_fma_f32 v[144:145], v[144:145], s[20:21], v[174:175] op_sel_hi:[1,0,0]
	s_waitcnt vmcnt(0)
	v_pk_mul_f32 v[204:205], v[204:205], v[176:177]
	v_mul_f32_e32 v146, 0x4b800000, v145
	v_cmp_gt_f32_e64 s[0:1], s36, v145
	v_cmp_gt_f32_e64 s[2:3], s36, v144
	v_pk_mul_f32 v[202:203], v[202:203], v[178:179]
	v_cndmask_b32_e64 v145, v145, v146, s[0:1]
	v_mul_f32_e32 v146, 0x4b800000, v144
	v_rsq_f32_e32 v145, v145
	v_cndmask_b32_e64 v144, v144, v146, s[2:3]
	v_rsq_f32_e32 v144, v144
	v_pk_mul_f32 v[132:133], v[132:133], v[182:183] op_sel_hi:[1,0]
	v_mul_f32_e32 v146, 0x45800000, v145
	v_cndmask_b32_e64 v184, v145, v146, s[0:1]
	v_mul_f32_e32 v145, 0x45800000, v144
	v_cndmask_b32_e64 v150, v144, v145, s[2:3]
	ds_read_b128 v[144:147], v196
	ds_read_b128 v[210:213], v196 offset:5120
	v_pk_mul_f32 v[134:135], v[134:135], v[182:183] op_sel_hi:[1,0]
	v_pk_mul_f32 v[206:207], v[128:129], v[180:181] op_sel_hi:[1,0]
	v_pk_mul_f32 v[208:209], v[130:131], v[180:181] op_sel_hi:[1,0]
	s_waitcnt lgkmcnt(1)
	v_pk_fma_f32 v[134:135], v[134:135], v[204:205], v[146:147]
	v_pk_fma_f32 v[132:133], v[132:133], v[202:203], v[144:145]
	v_pk_fma_f32 v[208:209], v[208:209], v[204:205], v[146:147]
	v_cvt_pk_bf16_f32 v132, v132, v133
	v_cvt_pk_bf16_f32 v133, v134, v135
	v_lshl_add_u64 v[134:135], v[158:159], 0, v[168:169]
	global_store_dwordx2 v[134:135], v[132:133], off
	v_pk_mul_f32 v[132:133], v[136:137], v[184:185] op_sel_hi:[1,0]
	v_pk_mul_f32 v[134:135], v[138:139], v[184:185] op_sel_hi:[1,0]
	v_pk_fma_f32 v[132:133], v[202:203], v[132:133], v[144:145]
	v_pk_fma_f32 v[134:135], v[204:205], v[134:135], v[146:147]
	v_cvt_pk_bf16_f32 v132, v132, v133
	v_cvt_pk_bf16_f32 v133, v134, v135
	v_lshl_add_u64 v[134:135], v[158:159], 0, v[170:171]
	v_pk_fma_f32 v[206:207], v[206:207], v[202:203], v[144:145]
	global_store_dwordx2 v[134:135], v[132:133], off
	v_pk_mul_f32 v[132:133], v[140:141], v[150:151] op_sel_hi:[1,0]
	v_pk_mul_f32 v[134:135], v[142:143], v[150:151] op_sel_hi:[1,0]
	v_cvt_pk_bf16_f32 v206, v206, v207
	v_cvt_pk_bf16_f32 v207, v208, v209
	v_lshlrev_b64 v[208:209], 11, v[166:167]
	v_pk_fma_f32 v[134:135], v[204:205], v[134:135], v[146:147]
	v_pk_fma_f32 v[132:133], v[202:203], v[132:133], v[144:145]
	v_lshlrev_b64 v[140:141], 11, v[172:173]
	v_lshl_add_u64 v[214:215], v[158:159], 0, v[208:209]
	v_cvt_pk_bf16_f32 v132, v132, v133
	v_cvt_pk_bf16_f32 v133, v134, v135
	v_lshl_add_u64 v[134:135], v[158:159], 0, v[140:141]
	global_store_dwordx2 v[214:215], v[206:207], off
	global_store_dwordx2 v[134:135], v[132:133], off
	global_load_dwordx4 v[136:139], v[156:157], off offset:1024
	ds_read_b128 v[128:131], v196 offset:1024
	s_waitcnt lgkmcnt(1)
	v_pk_add_f32 v[132:133], v[212:213], 1.0 op_sel_hi:[1,0]
	v_pk_add_f32 v[134:135], v[210:211], 1.0 op_sel_hi:[1,0]
	v_pk_mul_f32 v[124:125], v[124:125], v[180:181] op_sel_hi:[1,0]
	v_pk_mul_f32 v[126:127], v[126:127], v[180:181] op_sel_hi:[1,0]
	v_pk_mul_f32 v[112:113], v[112:113], v[182:183] op_sel_hi:[1,0]
	v_pk_mul_f32 v[114:115], v[114:115], v[182:183] op_sel_hi:[1,0]
	v_mov_b32_e32 v161, v151
	v_lshl_add_u64 v[172:173], s[16:17], 0, v[168:169]
	v_pk_mul_f32 v[100:101], v[100:101], v[182:183] op_sel_hi:[1,0]
	v_pk_mul_f32 v[102:103], v[102:103], v[182:183] op_sel_hi:[1,0]
	v_mov_b32_e32 v163, v151
	v_pk_mul_f32 v[84:85], v[84:85], v[180:181] op_sel_hi:[1,0]
	v_pk_mul_f32 v[86:87], v[86:87], v[180:181] op_sel_hi:[1,0]
	v_pk_mul_f32 v[88:89], v[88:89], v[182:183] op_sel_hi:[1,0]
	v_pk_mul_f32 v[90:91], v[90:91], v[182:183] op_sel_hi:[1,0]
	v_pk_mul_f32 v[80:81], v[80:81], v[150:151] op_sel_hi:[1,0]
	v_pk_mul_f32 v[82:83], v[82:83], v[150:151] op_sel_hi:[1,0]
	v_pk_mul_f32 v[92:93], v[92:93], v[184:185] op_sel_hi:[1,0]
	v_pk_mul_f32 v[94:95], v[94:95], v[184:185] op_sel_hi:[1,0]
	s_waitcnt vmcnt(0)
	v_pk_mul_f32 v[138:139], v[138:139], v[132:133]
	v_pk_mul_f32 v[136:137], v[136:137], v[134:135]
	s_waitcnt lgkmcnt(0)
	v_pk_fma_f32 v[126:127], v[126:127], v[138:139], v[130:131]
	v_pk_fma_f32 v[124:125], v[124:125], v[136:137], v[128:129]
	v_pk_fma_f32 v[114:115], v[114:115], v[138:139], v[130:131]
	v_pk_fma_f32 v[112:113], v[112:113], v[136:137], v[128:129]
	v_cvt_pk_bf16_f32 v124, v124, v125
	v_cvt_pk_bf16_f32 v125, v126, v127
	v_lshl_add_u64 v[126:127], s[16:17], 0, v[208:209]
	v_cvt_pk_bf16_f32 v112, v112, v113
	v_cvt_pk_bf16_f32 v113, v114, v115
	v_lshl_add_u64 v[114:115], v[172:173], 0, v[160:161]
	v_lshl_add_u64 v[142:143], v[126:127], 0, v[160:161]
	global_store_dwordx2 v[114:115], v[112:113], off
	v_pk_mul_f32 v[112:113], v[116:117], v[184:185] op_sel_hi:[1,0]
	v_pk_mul_f32 v[114:115], v[118:119], v[184:185] op_sel_hi:[1,0]
	global_store_dwordx2 v[142:143], v[124:125], off
	v_pk_fma_f32 v[114:115], v[114:115], v[138:139], v[130:131]
	v_pk_fma_f32 v[112:113], v[112:113], v[136:137], v[128:129]
	v_lshl_add_u64 v[124:125], s[16:17], 0, v[170:171]
	v_cvt_pk_bf16_f32 v112, v112, v113
	v_cvt_pk_bf16_f32 v113, v114, v115
	v_lshl_add_u64 v[114:115], v[124:125], 0, v[160:161]
	global_store_dwordx2 v[114:115], v[112:113], off
	v_pk_mul_f32 v[112:113], v[120:121], v[150:151] op_sel_hi:[1,0]
	v_pk_mul_f32 v[114:115], v[122:123], v[150:151] op_sel_hi:[1,0]
	v_pk_fma_f32 v[112:113], v[136:137], v[112:113], v[128:129]
	v_pk_fma_f32 v[114:115], v[138:139], v[114:115], v[130:131]
	v_lshl_add_u64 v[120:121], s[16:17], 0, v[140:141]
	v_cvt_pk_bf16_f32 v112, v112, v113
	v_cvt_pk_bf16_f32 v113, v114, v115
	v_lshl_add_u64 v[114:115], v[120:121], 0, v[160:161]
	global_store_dwordx2 v[114:115], v[112:113], off
	global_load_dwordx4 v[136:139], v[156:157], off offset:2048
	ds_read_b128 v[140:143], v196 offset:6144
	ds_read_b128 v[112:115], v196 offset:2048
	ds_read_b128 v[168:171], v196 offset:7168
	s_waitcnt lgkmcnt(2)
	v_pk_add_f32 v[116:117], v[142:143], 1.0 op_sel_hi:[1,0]
	v_pk_add_f32 v[118:119], v[140:141], 1.0 op_sel_hi:[1,0]
	v_pk_mul_f32 v[140:141], v[98:99], v[180:181] op_sel_hi:[1,0]
	s_waitcnt vmcnt(0)
	v_pk_mul_f32 v[122:123], v[138:139], v[116:117]
	v_pk_mul_f32 v[136:137], v[136:137], v[118:119]
	s_waitcnt lgkmcnt(1)
	v_pk_fma_f32 v[102:103], v[102:103], v[122:123], v[114:115]
	v_pk_fma_f32 v[100:101], v[100:101], v[136:137], v[112:113]
	v_pk_mul_f32 v[138:139], v[96:97], v[180:181] op_sel_hi:[1,0]
	v_cvt_pk_bf16_f32 v100, v100, v101
	v_cvt_pk_bf16_f32 v101, v102, v103
	v_lshl_add_u64 v[102:103], v[172:173], 0, v[162:163]
	global_store_dwordx2 v[102:103], v[100:101], off
	v_pk_mul_f32 v[100:101], v[104:105], v[184:185] op_sel_hi:[1,0]
	v_pk_mul_f32 v[102:103], v[106:107], v[184:185] op_sel_hi:[1,0]
	v_pk_fma_f32 v[100:101], v[100:101], v[136:137], v[112:113]
	v_pk_fma_f32 v[102:103], v[102:103], v[122:123], v[114:115]
	v_cvt_pk_bf16_f32 v100, v100, v101
	v_cvt_pk_bf16_f32 v101, v102, v103
	v_lshl_add_u64 v[102:103], v[124:125], 0, v[162:163]
	global_store_dwordx2 v[102:103], v[100:101], off
	v_pk_mul_f32 v[100:101], v[108:109], v[150:151] op_sel_hi:[1,0]
	v_pk_mul_f32 v[102:103], v[110:111], v[150:151] op_sel_hi:[1,0]
	v_pk_fma_f32 v[140:141], v[140:141], v[122:123], v[114:115]
	v_pk_fma_f32 v[138:139], v[138:139], v[136:137], v[112:113]
	v_pk_fma_f32 v[102:103], v[102:103], v[122:123], v[114:115]
	v_pk_fma_f32 v[100:101], v[100:101], v[136:137], v[112:113]
	v_cvt_pk_bf16_f32 v138, v138, v139
	v_cvt_pk_bf16_f32 v139, v140, v141
	v_lshl_add_u64 v[140:141], v[126:127], 0, v[162:163]
	v_cvt_pk_bf16_f32 v100, v100, v101
	v_cvt_pk_bf16_f32 v101, v102, v103
	v_lshl_add_u64 v[102:103], v[120:121], 0, v[162:163]
	global_store_dwordx2 v[140:141], v[138:139], off
	global_store_dwordx2 v[102:103], v[100:101], off
	global_load_dwordx4 v[104:107], v[156:157], off offset:3072
	ds_read_b128 v[96:99], v196 offset:3072
	s_waitcnt lgkmcnt(1)
	v_pk_add_f32 v[100:101], v[170:171], 1.0 op_sel_hi:[1,0]
	v_pk_add_f32 v[102:103], v[168:169], 1.0 op_sel_hi:[1,0]
	v_lshl_add_u64 v[110:111], v[126:127], 0, v[164:165]
	v_lshl_add_u64 v[122:123], v[172:173], 0, v[164:165]
	v_mov_b32_e32 v108, v76
	v_mov_b32_e32 v109, v60
	s_waitcnt vmcnt(0)
	v_pk_mul_f32 v[106:107], v[106:107], v[100:101]
	v_pk_mul_f32 v[104:105], v[104:105], v[102:103]
	s_waitcnt lgkmcnt(0)
	v_pk_fma_f32 v[86:87], v[86:87], v[106:107], v[98:99]
	v_pk_fma_f32 v[84:85], v[84:85], v[104:105], v[96:97]
	v_pk_fma_f32 v[90:91], v[90:91], v[106:107], v[98:99]
	v_pk_fma_f32 v[88:89], v[88:89], v[104:105], v[96:97]
	v_cvt_pk_bf16_f32 v84, v84, v85
	v_cvt_pk_bf16_f32 v85, v86, v87
	v_cvt_pk_bf16_f32 v86, v88, v89
	v_cvt_pk_bf16_f32 v87, v90, v91
	global_store_dwordx2 v[110:111], v[84:85], off
	global_store_dwordx2 v[122:123], v[86:87], off
	v_mov_b32_e32 v84, v77
	v_mov_b32_e32 v85, v61
	v_pk_mul_f32 v[84:85], v[84:85], v[84:85]
	v_mov_b32_e32 v86, v78
	v_pk_fma_f32 v[84:85], v[108:109], v[108:109], v[84:85]
	v_mov_b32_e32 v87, v62
	v_pk_fma_f32 v[84:85], v[86:87], v[86:87], v[84:85]
	v_mov_b32_e32 v86, v79
	v_mov_b32_e32 v87, v63
	v_mov_b32_e32 v88, v45
	v_mov_b32_e32 v89, v21
	v_pk_fma_f32 v[84:85], v[86:87], v[86:87], v[84:85]
	v_mov_b32_e32 v86, v44
	v_mov_b32_e32 v87, v20
	v_pk_mul_f32 v[88:89], v[88:89], v[88:89]
	v_mov_b32_e32 v90, v73
	v_pk_fma_f32 v[86:87], v[86:87], v[86:87], v[88:89]
	v_mov_b32_e32 v88, v46
	v_mov_b32_e32 v89, v22
	v_pk_fma_f32 v[86:87], v[88:89], v[88:89], v[86:87]
	v_mov_b32_e32 v88, v47
	v_mov_b32_e32 v89, v23
	v_mov_b32_e32 v91, v57
	v_pk_fma_f32 v[86:87], v[88:89], v[88:89], v[86:87]
	v_mov_b32_e32 v88, v72
	v_mov_b32_e32 v89, v56
	v_pk_mul_f32 v[90:91], v[90:91], v[90:91]
	v_mov_b32_e32 v108, v41
	v_pk_fma_f32 v[88:89], v[88:89], v[88:89], v[90:91]
	v_mov_b32_e32 v90, v74
	v_mov_b32_e32 v91, v58
	v_pk_fma_f32 v[88:89], v[90:91], v[90:91], v[88:89]
	v_mov_b32_e32 v90, v75
	v_mov_b32_e32 v91, v59
	v_mov_b32_e32 v109, v25
	v_pk_fma_f32 v[88:89], v[90:91], v[90:91], v[88:89]
	v_mov_b32_e32 v90, v40
	v_mov_b32_e32 v91, v24
	v_pk_mul_f32 v[108:109], v[108:109], v[108:109]
	v_pk_fma_f32 v[82:83], v[82:83], v[106:107], v[98:99]
	v_pk_fma_f32 v[80:81], v[80:81], v[104:105], v[96:97]
	v_pk_fma_f32 v[90:91], v[90:91], v[90:91], v[108:109]
	v_mov_b32_e32 v108, v42
	v_mov_b32_e32 v109, v26
	v_cvt_pk_bf16_f32 v80, v80, v81
	v_cvt_pk_bf16_f32 v81, v82, v83
	v_lshl_add_u64 v[82:83], v[120:121], 0, v[164:165]
	v_pk_fma_f32 v[90:91], v[108:109], v[108:109], v[90:91]
	v_mov_b32_e32 v108, v43
	v_mov_b32_e32 v109, v27
	global_store_dwordx2 v[82:83], v[80:81], off
	v_mov_b32_e32 v82, v69
	v_mov_b32_e32 v83, v53
	v_pk_fma_f32 v[90:91], v[108:109], v[108:109], v[90:91]
	v_mov_b32_e32 v108, v88
	v_mov_b32_e32 v109, v84
	v_mov_b32_e32 v84, v89
	v_mov_b32_e32 v80, v68
	v_mov_b32_e32 v81, v52
	v_pk_mul_f32 v[82:83], v[82:83], v[82:83]
	v_pk_fma_f32 v[94:95], v[94:95], v[106:107], v[98:99]
	v_pk_fma_f32 v[92:93], v[92:93], v[104:105], v[96:97]
	v_pk_add_f32 v[84:85], v[108:109], v[84:85]
	v_mov_b32_e32 v88, v90
	v_mov_b32_e32 v89, v86
	v_pk_fma_f32 v[80:81], v[80:81], v[80:81], v[82:83]
	v_mov_b32_e32 v82, v70
	v_mov_b32_e32 v83, v54
	v_pk_add_f32 v[84:85], v[84:85], v[88:89]
	v_mov_b32_e32 v86, v91
	v_cvt_pk_bf16_f32 v88, v92, v93
	v_cvt_pk_bf16_f32 v89, v94, v95
	v_lshl_add_u64 v[90:91], v[124:125], 0, v[164:165]
	v_pk_fma_f32 v[80:81], v[82:83], v[82:83], v[80:81]
	v_mov_b32_e32 v82, v71
	v_mov_b32_e32 v83, v55
	global_store_dwordx2 v[90:91], v[88:89], off
	v_pk_fma_f32 v[88:89], v[82:83], v[82:83], v[80:81]
	v_mov_b32_e32 v82, v37
	v_mov_b32_e32 v83, v29
	v_mov_b32_e32 v80, v36
	v_mov_b32_e32 v81, v28
	v_pk_mul_f32 v[82:83], v[82:83], v[82:83]
	v_pk_add_f32 v[84:85], v[84:85], v[86:87]
	v_pk_fma_f32 v[80:81], v[80:81], v[80:81], v[82:83]
	v_mov_b32_e32 v82, v38
	v_mov_b32_e32 v83, v30
	v_pk_fma_f32 v[80:81], v[82:83], v[82:83], v[80:81]
	v_mov_b32_e32 v82, v39
	v_mov_b32_e32 v83, v31
	v_pk_fma_f32 v[90:91], v[82:83], v[82:83], v[80:81]
	v_mov_b32_e32 v82, v65
	v_mov_b32_e32 v83, v49
	v_mov_b32_e32 v80, v64
	v_mov_b32_e32 v81, v48
	v_pk_mul_f32 v[82:83], v[82:83], v[82:83]
	ds_bpermute_b32 v87, v189, v85
	v_pk_fma_f32 v[80:81], v[80:81], v[80:81], v[82:83]
	v_mov_b32_e32 v82, v66
	v_mov_b32_e32 v83, v50
	v_pk_fma_f32 v[92:93], v[82:83], v[82:83], v[80:81]
	global_load_dwordx4 v[80:83], v[156:157], off
	ds_bpermute_b32 v86, v189, v84
	v_mov_b32_e32 v94, v67
	v_mov_b32_e32 v95, v51
	v_mov_b32_e32 v104, v33
	v_mov_b32_e32 v105, v17
	s_waitcnt lgkmcnt(0)
	v_pk_add_f32 v[84:85], v[84:85], v[86:87]
	ds_bpermute_b32 v87, v190, v85
	ds_bpermute_b32 v86, v190, v84
	v_pk_fma_f32 v[92:93], v[94:95], v[94:95], v[92:93]
	v_mov_b32_e32 v94, v32
	v_mov_b32_e32 v95, v16
	v_pk_mul_f32 v[104:105], v[104:105], v[104:105]
	s_waitcnt lgkmcnt(0)
	v_pk_add_f32 v[84:85], v[84:85], v[86:87]
	ds_bpermute_b32 v87, v191, v85
	ds_bpermute_b32 v86, v191, v84
	v_pk_fma_f32 v[94:95], v[94:95], v[94:95], v[104:105]
	v_mov_b32_e32 v104, v34
	v_mov_b32_e32 v105, v18
	v_pk_fma_f32 v[94:95], v[104:105], v[104:105], v[94:95]
	v_mov_b32_e32 v104, v35
	v_mov_b32_e32 v105, v19
	v_pk_fma_f32 v[94:95], v[104:105], v[104:105], v[94:95]
	v_mov_b32_e32 v104, v92
	v_mov_b32_e32 v105, v88
	v_mov_b32_e32 v88, v93
	v_pk_add_f32 v[88:89], v[104:105], v[88:89]
	v_mov_b32_e32 v92, v94
	v_mov_b32_e32 v93, v90
	v_pk_add_f32 v[88:89], v[88:89], v[92:93]
	v_mov_b32_e32 v90, v95
	s_waitcnt lgkmcnt(0)
	v_pk_add_f32 v[84:85], v[84:85], v[86:87]
	v_pk_add_f32 v[88:89], v[88:89], v[90:91]
	ds_bpermute_b32 v87, v192, v85
	ds_bpermute_b32 v86, v192, v84
	ds_bpermute_b32 v91, v189, v89
	ds_bpermute_b32 v90, v189, v88
	v_or_b32_e32 v92, 4, v166
	v_ashrrev_i32_e32 v93, 31, v92
	s_waitcnt lgkmcnt(2)
	v_pk_add_f32 v[84:85], v[84:85], v[86:87]
	ds_bpermute_b32 v87, v193, v85
	s_waitcnt lgkmcnt(1)
	v_pk_add_f32 v[88:89], v[88:89], v[90:91]
	ds_bpermute_b32 v86, v193, v84
	ds_bpermute_b32 v91, v190, v89
	ds_bpermute_b32 v90, v190, v88
	s_waitcnt lgkmcnt(2)
	v_pk_add_f32 v[84:85], v[84:85], v[86:87]
	ds_bpermute_b32 v87, v194, v85
	s_waitcnt lgkmcnt(1)
	v_pk_add_f32 v[88:89], v[88:89], v[90:91]
	ds_bpermute_b32 v86, v194, v84
	ds_bpermute_b32 v91, v191, v89
	ds_bpermute_b32 v90, v191, v88
	s_waitcnt lgkmcnt(2)
	v_pk_add_f32 v[84:85], v[84:85], v[86:87]
	s_nop 0
	v_pk_fma_f32 v[84:85], v[84:85], s[20:21], v[174:175] op_sel_hi:[1,0,0]
	s_waitcnt lgkmcnt(0)
	v_pk_add_f32 v[86:87], v[88:89], v[90:91]
	ds_bpermute_b32 v89, v192, v87
	ds_bpermute_b32 v88, v192, v86
	v_mul_f32_e32 v90, 0x4b800000, v85
	v_cmp_gt_f32_e64 s[0:1], s36, v85
	v_cmp_gt_f32_e64 s[2:3], s36, v84
	s_waitcnt lgkmcnt(0)
	v_pk_add_f32 v[86:87], v[86:87], v[88:89]
	ds_bpermute_b32 v89, v193, v87
	ds_bpermute_b32 v88, v193, v86
	v_cndmask_b32_e64 v85, v85, v90, s[0:1]
	v_rsq_f32_e32 v90, v85
	v_mul_f32_e32 v85, 0x4b800000, v84
	v_cndmask_b32_e64 v84, v84, v85, s[2:3]
	v_rsq_f32_e32 v91, v84
	s_waitcnt lgkmcnt(0)
	v_pk_add_f32 v[84:85], v[86:87], v[88:89]
	ds_bpermute_b32 v87, v194, v85
	ds_bpermute_b32 v86, v194, v84
	v_mul_f32_e32 v88, 0x45800000, v90
	v_cndmask_b32_e64 v88, v90, v88, s[0:1]
	v_mul_f32_e32 v89, 0x45800000, v91
	v_pk_mul_f32 v[76:77], v[76:77], v[88:89] op_sel_hi:[1,0]
	s_waitcnt lgkmcnt(0)
	v_pk_add_f32 v[84:85], v[84:85], v[86:87]
	s_waitcnt vmcnt(0)
	v_pk_mul_f32 v[82:83], v[176:177], v[82:83]
	v_pk_fma_f32 v[84:85], v[84:85], s[20:21], v[174:175] op_sel_hi:[1,0,0]
	v_pk_mul_f32 v[80:81], v[178:179], v[80:81]
	v_mul_f32_e32 v86, 0x4b800000, v85
	v_cmp_gt_f32_e64 s[0:1], s36, v85
	v_cmp_gt_f32_e64 s[4:5], s36, v84
	v_pk_mul_f32 v[78:79], v[78:79], v[88:89] op_sel_hi:[1,0]
	v_cndmask_b32_e64 v85, v85, v86, s[0:1]
	v_mul_f32_e32 v86, 0x4b800000, v84
	v_rsq_f32_e32 v85, v85
	v_cndmask_b32_e64 v84, v84, v86, s[4:5]
	v_rsq_f32_e32 v87, v84
	v_pk_fma_f32 v[78:79], v[78:79], v[82:83], v[146:147]
	v_pk_fma_f32 v[76:77], v[76:77], v[80:81], v[144:145]
	v_mul_f32_e32 v86, 0x45800000, v85
	v_cvt_pk_bf16_f32 v76, v76, v77
	v_cvt_pk_bf16_f32 v77, v78, v79
	v_lshlrev_b64 v[78:79], 11, v[92:93]
	v_cndmask_b32_e64 v84, v91, v89, s[2:3]
	v_cndmask_b32_e64 v86, v85, v86, s[0:1]
	v_mul_f32_e32 v85, 0x45800000, v87
	v_lshl_add_u64 v[92:93], v[158:159], 0, v[78:79]
	global_store_dwordx2 v[92:93], v[76:77], off
	v_or_b32_e32 v76, 5, v166
	v_pk_mul_f32 v[72:73], v[72:73], v[84:85] op_sel_hi:[1,0]
	v_pk_mul_f32 v[74:75], v[74:75], v[84:85] op_sel_hi:[1,0]
	v_pk_fma_f32 v[72:73], v[72:73], v[80:81], v[144:145]
	v_pk_fma_f32 v[74:75], v[74:75], v[82:83], v[146:147]
	v_ashrrev_i32_e32 v77, 31, v76
	v_cvt_pk_bf16_f32 v72, v72, v73
	v_cvt_pk_bf16_f32 v73, v74, v75
	v_lshlrev_b64 v[74:75], 11, v[76:77]
	v_lshl_add_u64 v[76:77], v[158:159], 0, v[74:75]
	global_store_dwordx2 v[76:77], v[72:73], off
	v_or_b32_e32 v72, 6, v166
	v_pk_mul_f32 v[68:69], v[68:69], v[86:87] op_sel_hi:[1,0]
	v_pk_mul_f32 v[70:71], v[70:71], v[86:87] op_sel_hi:[1,0]
	v_pk_fma_f32 v[68:69], v[80:81], v[68:69], v[144:145]
	v_pk_fma_f32 v[70:71], v[82:83], v[70:71], v[146:147]
	v_ashrrev_i32_e32 v73, 31, v72
	v_cvt_pk_bf16_f32 v68, v68, v69
	v_cvt_pk_bf16_f32 v69, v70, v71
	v_lshlrev_b64 v[70:71], 11, v[72:73]
	v_lshl_add_u64 v[72:73], v[158:159], 0, v[70:71]
	v_cndmask_b32_e64 v90, v87, v85, s[4:5]
	global_store_dwordx2 v[72:73], v[68:69], off
	v_or_b32_e32 v68, 7, v166
	v_pk_mul_f32 v[64:65], v[64:65], v[90:91] op_sel_hi:[1,0]
	v_pk_mul_f32 v[66:67], v[66:67], v[90:91] op_sel_hi:[1,0]
	v_ashrrev_i32_e32 v69, 31, v68
	v_pk_fma_f32 v[66:67], v[82:83], v[66:67], v[146:147]
	v_pk_fma_f32 v[64:65], v[80:81], v[64:65], v[144:145]
	v_lshlrev_b64 v[68:69], 11, v[68:69]
	v_cvt_pk_bf16_f32 v64, v64, v65
	v_cvt_pk_bf16_f32 v65, v66, v67
	v_lshl_add_u64 v[66:67], v[158:159], 0, v[68:69]
	global_store_dwordx2 v[66:67], v[64:65], off
	global_load_dwordx4 v[64:67], v[156:157], off offset:1024
	v_pk_mul_f32 v[60:61], v[60:61], v[88:89] op_sel_hi:[1,0]
	v_pk_mul_f32 v[62:63], v[62:63], v[88:89] op_sel_hi:[1,0]
	v_pk_mul_f32 v[56:57], v[56:57], v[84:85] op_sel_hi:[1,0]
	v_pk_mul_f32 v[58:59], v[58:59], v[84:85] op_sel_hi:[1,0]
	v_pk_mul_f32 v[52:53], v[52:53], v[86:87] op_sel_hi:[1,0]
	v_pk_mul_f32 v[54:55], v[54:55], v[86:87] op_sel_hi:[1,0]
	v_pk_mul_f32 v[48:49], v[48:49], v[90:91] op_sel_hi:[1,0]
	v_pk_mul_f32 v[50:51], v[50:51], v[90:91] op_sel_hi:[1,0]
	v_pk_mul_f32 v[44:45], v[44:45], v[88:89] op_sel_hi:[1,0]
	v_pk_mul_f32 v[46:47], v[46:47], v[88:89] op_sel_hi:[1,0]
	v_pk_mul_f32 v[40:41], v[40:41], v[84:85] op_sel_hi:[1,0]
	v_pk_mul_f32 v[42:43], v[42:43], v[84:85] op_sel_hi:[1,0]
	v_pk_mul_f32 v[36:37], v[36:37], v[86:87] op_sel_hi:[1,0]
	v_pk_mul_f32 v[38:39], v[38:39], v[86:87] op_sel_hi:[1,0]
	v_pk_mul_f32 v[32:33], v[32:33], v[90:91] op_sel_hi:[1,0]
	v_pk_mul_f32 v[34:35], v[34:35], v[90:91] op_sel_hi:[1,0]
	v_pk_mul_f32 v[20:21], v[20:21], v[88:89] op_sel_hi:[1,0]
	v_pk_mul_f32 v[22:23], v[22:23], v[88:89] op_sel_hi:[1,0]
	v_pk_mul_f32 v[16:17], v[16:17], v[90:91] op_sel_hi:[1,0]
	v_pk_mul_f32 v[18:19], v[18:19], v[90:91] op_sel_hi:[1,0]
	v_pk_mul_f32 v[24:25], v[24:25], v[84:85] op_sel_hi:[1,0]
	v_pk_mul_f32 v[26:27], v[26:27], v[84:85] op_sel_hi:[1,0]
	v_pk_mul_f32 v[28:29], v[28:29], v[86:87] op_sel_hi:[1,0]
	v_pk_mul_f32 v[30:31], v[30:31], v[86:87] op_sel_hi:[1,0]
	s_waitcnt vmcnt(0)
	v_pk_mul_f32 v[66:67], v[132:133], v[66:67]
	v_pk_mul_f32 v[64:65], v[134:135], v[64:65]
	v_pk_fma_f32 v[62:63], v[62:63], v[66:67], v[130:131]
	v_pk_fma_f32 v[60:61], v[60:61], v[64:65], v[128:129]
	v_pk_fma_f32 v[58:59], v[58:59], v[66:67], v[130:131]
	v_cvt_pk_bf16_f32 v60, v60, v61
	v_cvt_pk_bf16_f32 v61, v62, v63
	v_lshl_add_u64 v[62:63], s[16:17], 0, v[78:79]
	v_pk_fma_f32 v[56:57], v[56:57], v[64:65], v[128:129]
	v_lshl_add_u64 v[72:73], v[62:63], 0, v[160:161]
	v_cvt_pk_bf16_f32 v56, v56, v57
	v_cvt_pk_bf16_f32 v57, v58, v59
	v_lshl_add_u64 v[58:59], s[16:17], 0, v[74:75]
	v_pk_fma_f32 v[54:55], v[54:55], v[66:67], v[130:131]
	v_pk_fma_f32 v[52:53], v[52:53], v[64:65], v[128:129]
	global_store_dwordx2 v[72:73], v[60:61], off
	v_lshl_add_u64 v[60:61], v[58:59], 0, v[160:161]
	v_cvt_pk_bf16_f32 v52, v52, v53
	v_cvt_pk_bf16_f32 v53, v54, v55
	v_lshl_add_u64 v[54:55], s[16:17], 0, v[70:71]
	global_store_dwordx2 v[60:61], v[56:57], off
	v_lshl_add_u64 v[56:57], v[54:55], 0, v[160:161]
	global_store_dwordx2 v[56:57], v[52:53], off
	v_pk_fma_f32 v[50:51], v[66:67], v[50:51], v[130:131]
	v_pk_fma_f32 v[48:49], v[64:65], v[48:49], v[128:129]
	v_lshl_add_u64 v[52:53], s[16:17], 0, v[68:69]
	v_cvt_pk_bf16_f32 v48, v48, v49
	v_cvt_pk_bf16_f32 v49, v50, v51
	v_lshl_add_u64 v[50:51], v[52:53], 0, v[160:161]
	global_store_dwordx2 v[50:51], v[48:49], off
	global_load_dwordx4 v[48:51], v[156:157], off offset:2048
	s_waitcnt vmcnt(0)
	v_pk_mul_f32 v[50:51], v[116:117], v[50:51]
	v_pk_mul_f32 v[48:49], v[118:119], v[48:49]
	v_pk_fma_f32 v[46:47], v[46:47], v[50:51], v[114:115]
	v_pk_fma_f32 v[44:45], v[44:45], v[48:49], v[112:113]
	v_pk_fma_f32 v[42:43], v[42:43], v[50:51], v[114:115]
	v_pk_fma_f32 v[40:41], v[40:41], v[48:49], v[112:113]
	v_pk_fma_f32 v[38:39], v[38:39], v[50:51], v[114:115]
	v_pk_fma_f32 v[36:37], v[36:37], v[48:49], v[112:113]
	v_pk_fma_f32 v[34:35], v[50:51], v[34:35], v[114:115]
	v_pk_fma_f32 v[32:33], v[48:49], v[32:33], v[112:113]
	v_cvt_pk_bf16_f32 v44, v44, v45
	v_cvt_pk_bf16_f32 v45, v46, v47
	v_lshl_add_u64 v[46:47], v[62:63], 0, v[162:163]
	v_cvt_pk_bf16_f32 v40, v40, v41
	v_cvt_pk_bf16_f32 v41, v42, v43
	v_lshl_add_u64 v[42:43], v[58:59], 0, v[162:163]
	v_cvt_pk_bf16_f32 v36, v36, v37
	v_cvt_pk_bf16_f32 v37, v38, v39
	v_lshl_add_u64 v[38:39], v[54:55], 0, v[162:163]
	v_cvt_pk_bf16_f32 v32, v32, v33
	v_cvt_pk_bf16_f32 v33, v34, v35
	v_lshl_add_u64 v[34:35], v[52:53], 0, v[162:163]
	global_store_dwordx2 v[46:47], v[44:45], off
	global_store_dwordx2 v[42:43], v[40:41], off
	global_store_dwordx2 v[38:39], v[36:37], off
	global_store_dwordx2 v[34:35], v[32:33], off
	global_load_dwordx4 v[32:35], v[156:157], off offset:3072
	v_lshl_add_u64 v[36:37], v[62:63], 0, v[164:165]
	v_lshl_add_u64 v[38:39], v[58:59], 0, v[164:165]
	v_lshl_add_u64 v[40:41], v[54:55], 0, v[164:165]
	s_waitcnt vmcnt(0)
	v_pk_mul_f32 v[34:35], v[100:101], v[34:35]
	v_pk_mul_f32 v[32:33], v[102:103], v[32:33]
	v_pk_fma_f32 v[22:23], v[22:23], v[34:35], v[98:99]
	v_pk_fma_f32 v[20:21], v[20:21], v[32:33], v[96:97]
	v_pk_fma_f32 v[18:19], v[18:19], v[34:35], v[98:99]
	v_pk_fma_f32 v[16:17], v[16:17], v[32:33], v[96:97]
	v_pk_fma_f32 v[26:27], v[26:27], v[34:35], v[98:99]
	v_pk_fma_f32 v[24:25], v[24:25], v[32:33], v[96:97]
	v_pk_fma_f32 v[30:31], v[30:31], v[34:35], v[98:99]
	v_pk_fma_f32 v[28:29], v[28:29], v[32:33], v[96:97]
	v_cvt_pk_bf16_f32 v20, v20, v21
	v_cvt_pk_bf16_f32 v21, v22, v23
	v_cvt_pk_bf16_f32 v16, v16, v17
	v_cvt_pk_bf16_f32 v17, v18, v19
	v_lshl_add_u64 v[18:19], v[52:53], 0, v[164:165]
	v_cvt_pk_bf16_f32 v22, v24, v25
	v_cvt_pk_bf16_f32 v23, v26, v27
	v_cvt_pk_bf16_f32 v24, v28, v29
	v_cvt_pk_bf16_f32 v25, v30, v31
	global_store_dwordx2 v[36:37], v[20:21], off
	global_store_dwordx2 v[38:39], v[22:23], off
	global_store_dwordx2 v[40:41], v[24:25], off
	global_store_dwordx2 v[18:19], v[16:17], off
	s_and_saveexec_b64 s[2:3], s[8:9]
	s_cbranch_execz .LBB0_142
	global_load_dwordx4 v[16:19], v[156:157], off
	v_mov_b32_e32 v22, v13
	v_mov_b32_e32 v23, v9
	v_mov_b32_e32 v20, v12
	v_mov_b32_e32 v21, v8
	v_mov_b32_e32 v30, v5
	v_mov_b32_e32 v31, v1
	v_pk_mul_f32 v[22:23], v[22:23], v[22:23]
	v_mov_b32_e32 v24, v14
	v_mov_b32_e32 v25, v10
	v_mov_b32_e32 v28, v4
	v_mov_b32_e32 v29, v0
	v_pk_mul_f32 v[30:31], v[30:31], v[30:31]
	v_pk_fma_f32 v[20:21], v[20:21], v[20:21], v[22:23]
	v_mov_b32_e32 v26, v15
	v_mov_b32_e32 v27, v11
	v_mov_b32_e32 v32, v6
	v_mov_b32_e32 v33, v2
	v_pk_fma_f32 v[22:23], v[28:29], v[28:29], v[30:31]
	v_pk_fma_f32 v[20:21], v[24:25], v[24:25], v[20:21]
	v_mov_b32_e32 v34, v7
	v_mov_b32_e32 v35, v3
	v_pk_fma_f32 v[22:23], v[32:33], v[32:33], v[22:23]
	v_pk_fma_f32 v[20:21], v[26:27], v[26:27], v[20:21]
	v_pk_fma_f32 v[22:23], v[34:35], v[34:35], v[22:23]
	v_add_f32_e32 v20, v20, v21
	v_add_f32_e32 v20, v20, v22
	v_add_f32_e32 v20, v20, v23
	ds_bpermute_b32 v21, v189, v20
	v_add_u32_e32 v36, s38, v195
	v_ashrrev_i32_e32 v37, 31, v36
	v_lshlrev_b64 v[36:37], 11, v[36:37]
	v_lshl_add_u64 v[36:37], v[158:159], 0, v[36:37]
	s_waitcnt lgkmcnt(0)
	v_add_f32_e32 v20, v20, v21
	ds_bpermute_b32 v21, v190, v20
	s_waitcnt lgkmcnt(0)
	v_add_f32_e32 v20, v20, v21
	ds_bpermute_b32 v21, v191, v20
	s_waitcnt lgkmcnt(0)
	v_add_f32_e32 v20, v20, v21
	ds_bpermute_b32 v21, v192, v20
	s_waitcnt lgkmcnt(0)
	v_add_f32_e32 v28, v20, v21
	ds_bpermute_b32 v29, v193, v28
	ds_read_b128 v[20:23], v196 offset:8192
	ds_read_b128 v[24:27], v196 offset:9216
	s_waitcnt lgkmcnt(2)
	v_add_f32_e32 v38, v28, v29
	ds_bpermute_b32 v39, v194, v38
	ds_read_b128 v[28:31], v196 offset:12288
	ds_read_b128 v[32:35], v196 offset:13312
	s_waitcnt lgkmcnt(2)
	v_add_f32_e32 v38, v38, v39
	v_fmamk_f32 v38, v38, 0x3a800000, v200
	v_mul_f32_e32 v39, 0x4b800000, v38
	v_cmp_gt_f32_e64 s[0:1], s36, v38
	s_waitcnt lgkmcnt(1)
	v_pk_add_f32 v[30:31], v[30:31], 1.0 op_sel_hi:[1,0]
	v_pk_add_f32 v[28:29], v[28:29], 1.0 op_sel_hi:[1,0]
	v_cndmask_b32_e64 v38, v38, v39, s[0:1]
	v_rsq_f32_e32 v38, v38
	s_waitcnt vmcnt(0)
	v_pk_mul_f32 v[18:19], v[18:19], v[30:31]
	v_mul_f32_e32 v39, 0x45800000, v38
	v_cndmask_b32_e64 v38, v38, v39, s[0:1]
	v_pk_mul_f32 v[12:13], v[12:13], v[38:39] op_sel_hi:[1,0]
	v_pk_mul_f32 v[14:15], v[14:15], v[38:39] op_sel_hi:[1,0]
	v_pk_mul_f32 v[16:17], v[16:17], v[28:29]
	v_pk_fma_f32 v[14:15], v[18:19], v[14:15], v[22:23]
	v_pk_fma_f32 v[12:13], v[16:17], v[12:13], v[20:21]
	s_waitcnt lgkmcnt(0)
	v_pk_add_f32 v[16:17], v[34:35], 1.0 op_sel_hi:[1,0]
	v_cvt_pk_bf16_f32 v12, v12, v13
	v_cvt_pk_bf16_f32 v13, v14, v15
	global_store_dwordx2 v[36:37], v[12:13], off
	global_load_dwordx4 v[12:15], v[156:157], off offset:1024
	v_pk_add_f32 v[18:19], v[32:33], 1.0 op_sel_hi:[1,0]
	v_pk_mul_f32 v[8:9], v[8:9], v[38:39] op_sel_hi:[1,0]
	v_pk_mul_f32 v[10:11], v[10:11], v[38:39] op_sel_hi:[1,0]
	v_pk_mul_f32 v[4:5], v[4:5], v[38:39] op_sel_hi:[1,0]
	v_pk_mul_f32 v[6:7], v[6:7], v[38:39] op_sel_hi:[1,0]
	v_pk_mul_f32 v[0:1], v[0:1], v[38:39] op_sel_hi:[1,0]
	v_pk_mul_f32 v[2:3], v[2:3], v[38:39] op_sel_hi:[1,0]
	s_waitcnt vmcnt(0)
	v_pk_mul_f32 v[14:15], v[14:15], v[16:17]
	v_pk_mul_f32 v[12:13], v[12:13], v[18:19]
	v_pk_fma_f32 v[10:11], v[14:15], v[10:11], v[26:27]
	v_pk_fma_f32 v[8:9], v[12:13], v[8:9], v[24:25]
	s_nop 0
	v_cvt_pk_bf16_f32 v8, v8, v9
	v_cvt_pk_bf16_f32 v9, v10, v11
	global_store_dwordx2 v[36:37], v[8:9], off offset:512
	global_load_dwordx4 v[8:11], v[156:157], off offset:2048
	ds_read_b128 v[12:15], v196 offset:14336
	ds_read_b128 v[16:19], v196 offset:10240
	ds_read_b128 v[20:23], v196 offset:11264
	ds_read_b128 v[24:27], v196 offset:15360
	s_waitcnt lgkmcnt(3)
	v_pk_add_f32 v[14:15], v[14:15], 1.0 op_sel_hi:[1,0]
	v_pk_add_f32 v[12:13], v[12:13], 1.0 op_sel_hi:[1,0]
	s_waitcnt vmcnt(0)
	v_pk_mul_f32 v[10:11], v[10:11], v[14:15]
	v_pk_mul_f32 v[8:9], v[8:9], v[12:13]
	s_waitcnt lgkmcnt(2)
	v_pk_fma_f32 v[6:7], v[6:7], v[10:11], v[18:19]
	v_pk_fma_f32 v[4:5], v[4:5], v[8:9], v[16:17]
	s_waitcnt lgkmcnt(0)
	v_pk_add_f32 v[8:9], v[26:27], 1.0 op_sel_hi:[1,0]
	v_cvt_pk_bf16_f32 v4, v4, v5
	v_cvt_pk_bf16_f32 v5, v6, v7
	global_store_dwordx2 v[36:37], v[4:5], off offset:1024
	global_load_dwordx4 v[4:7], v[156:157], off offset:3072
	v_pk_add_f32 v[10:11], v[24:25], 1.0 op_sel_hi:[1,0]
	s_waitcnt vmcnt(0)
	v_pk_mul_f32 v[6:7], v[6:7], v[8:9]
	v_pk_mul_f32 v[4:5], v[4:5], v[10:11]
	v_pk_fma_f32 v[2:3], v[2:3], v[6:7], v[22:23]
	v_pk_fma_f32 v[0:1], v[0:1], v[4:5], v[20:21]
	s_nop 0
	v_cvt_pk_bf16_f32 v0, v0, v1
	v_cvt_pk_bf16_f32 v1, v2, v3
	global_store_dwordx2 v[36:37], v[0:1], off offset:1536
	s_branch .LBB0_142
